# GEMM phases: one static s_setprio 1 for the second wave half (waves 4-7) for the whole phase instead of per-segment toggling
# speedup vs baseline: 1.0088x; 1.0005x over previous
.LBB0_261:
	v_readlane_b32 s4, v255, 12
	v_readlane_b32 s5, v255, 13
	s_mov_b32 s5, s56
	v_writelane_b32 v255, s4, 12
	s_mov_b32 s22, s2
	v_mov_b32_e32 v11, v0
	v_writelane_b32 v255, s5, 13
	s_cmpk_gt_i32 s22, 0x76f
	v_readfirstlane_b32 s23, v11
	s_cbranch_scc1 .LBB0_273
	v_lshlrev_b32_e32 v2, 4, v11
	v_add_u32_e32 v3, 0x2000, v2
	v_ashrrev_i32_e32 v4, 31, v3
	v_lshrrev_b32_e32 v4, 22, v4
	v_add_u32_e32 v4, v3, v4
	v_ashrrev_i32_e32 v4, 10, v4
	v_mul_i32_i24_e32 v5, 0x400, v4
	v_sub_u32_e32 v3, v3, v5
	v_lshrrev_b32_e32 v5, 4, v3
	v_bitop3_b32 v3, v5, v3, 32 bitop3:0x6c
	v_ashrrev_i32_e32 v6, 31, v3
	v_lshrrev_b32_e32 v6, 26, v6
	v_add_u32_e32 v6, v3, v6
	v_ashrrev_i32_e32 v7, 6, v6
	v_and_b32_e32 v6, 0xc0, v6
	v_sub_u32_e32 v3, v3, v6
	v_bfe_i32 v6, v11, 27, 1
	v_lshrrev_b32_e32 v6, 22, v6
	v_add_u32_e32 v6, v2, v6
	v_and_b32_e32 v6, 0xfffffc00, v6
	v_sub_u32_e32 v2, v2, v6
	v_lshlrev_b32_e32 v5, 5, v4
	v_lshrrev_b32_e32 v6, 4, v2
	v_and_b32_e32 v5, 32, v5
	v_ashrrev_i16_sdwa v3, v1, sext(v3) dst_sel:DWORD dst_unused:UNUSED_PAD src0_sel:DWORD src1_sel:BYTE_0
	v_bitop3_b32 v6, v6, v2, 32 bitop3:0x6c
	v_ashrrev_i32_e32 v2, 31, v2
	v_add_u32_sdwa v10, v5, sext(v3) dst_sel:DWORD dst_unused:UNUSED_PAD src0_sel:DWORD src1_sel:WORD_0
	v_ashrrev_i32_e32 v3, 31, v11
	v_lshrrev_b32_e32 v2, 26, v2
	s_load_dwordx2 s[4:5], s[0:1], 0x258
	s_load_dwordx4 s[8:11], s[0:1], 0x130
	v_lshrrev_b32_e32 v3, 26, v3
	v_add_u32_e32 v2, v6, v2
	v_add_u32_e32 v3, v11, v3
	v_ashrrev_i32_e32 v2, 6, v2
	v_readlane_b32 s6, v255, 12
	v_ashrrev_i32_e32 v3, 6, v3
	v_mul_i32_i24_e32 v8, 64, v2
	s_mul_i32 s1, s6, 0x700000
	v_lshlrev_b32_e32 v5, 5, v3
	v_sub_u32_e32 v6, v6, v8
	v_lshlrev_b32_e32 v4, 3, v4
	v_lshlrev_b32_e32 v3, 3, v3
	s_mul_hi_u32 s0, s6, 0x700000
	s_waitcnt lgkmcnt(0)
	s_add_u32 s24, s4, s1
	v_and_b32_e32 v5, 32, v5
	v_ashrrev_i16_sdwa v6, v1, sext(v6) dst_sel:DWORD dst_unused:UNUSED_PAD src0_sel:DWORD src1_sel:BYTE_0
	v_and_b32_e32 v4, -16, v4
	v_and_b32_e32 v3, -16, v3
	s_addc_u32 s25, s5, s0
	v_add_u32_sdwa v5, v5, sext(v6) dst_sel:DWORD dst_unused:UNUSED_PAD src0_sel:DWORD src1_sel:WORD_0
	v_add_u32_e32 v4, v7, v4
	v_and_b32_e32 v6, 3, v7
	s_mov_b32 s0, 0x1fffe0
	v_add_u32_e32 v3, v2, v3
	v_and_b32_e32 v2, 3, v2
	s_ashr_i32 s27, s22, 31
	v_and_or_b32 v6, v4, s0, v6
	v_and_or_b32 v2, v3, s0, v2
	s_lshr_b32 s0, s27, 29
	s_add_i32 s0, s22, s0
	s_ashr_i32 s4, s23, 6
	s_ashr_i32 s5, s0, 3
	s_and_b32 s0, s0, -8
	s_ashr_i32 s1, s23, 8
	s_lshl_b32 s26, s4, 10
	s_sub_i32 s0, s22, s0
	s_cmp_lt_i32 s0, 0
	s_movk_i32 s6, 0xef
	s_cselect_b32 s6, s6, 0xee
	s_mul_i32 s0, s6, s0
	s_add_i32 s0, s0, s5
	s_mul_hi_i32 s5, s0, 0x92492493
	s_add_i32 s5, s5, s0
	s_lshr_b32 s6, s5, 31
	s_ashr_i32 s5, s5, 6
	s_add_i32 s5, s5, s6
	s_lshl_b32 s6, s5, 3
	s_mulk_i32 s5, 0x70
	s_sub_i32 s5, s0, s5
	s_bfe_i32 s0, s5, 0x80000
	v_readlane_b32 s7, v255, 13
	s_bfe_u32 s0, s0, 0x3000c
	v_lshrrev_b32_e32 v7, 2, v4
	v_lshlrev_b32_e32 v8, 1, v4
	s_add_i32 s7, s5, s0
	v_and_b32_e32 v7, 4, v7
	v_and_b32_e32 v8, 24, v8
	s_bfe_i32 s0, s7, 0x80000
	s_and_b32 s7, s7, 0xf8
	v_or3_b32 v6, v6, v7, v8
	v_lshlrev_b32_e32 v7, 1, v10
	s_sub_i32 s5, s5, s7
	v_lshl_add_u32 v130, v6, 11, v7
	v_lshrrev_b32_e32 v6, 2, v3
	v_lshlrev_b32_e32 v7, 1, v3
	s_sext_i32_i16 s0, s0
	s_sext_i32_i8 s5, s5
	v_and_b32_e32 v6, 4, v6
	v_and_b32_e32 v7, 24, v7
	s_lshr_b32 s0, s0, 3
	s_add_i32 s39, s6, s5
	v_or3_b32 v2, v2, v6, v7
	v_lshlrev_b32_e32 v6, 1, v5
	s_lshl_b32 s5, s39, 18
	v_lshl_add_u32 v146, v3, 10, v5
	v_lshlrev_b32_e32 v12, 10, v4
	s_bfe_i64 s[6:7], s[0:1], 0x100000
	v_lshl_add_u32 v132, v2, 11, v6
	v_add_lshl_u32 v134, v146, s5, 1
	v_add_u32_e32 v2, s5, v12
	s_bitset1_b32 s5, 17
	s_lshl_b64 s[6:7], s[6:7], 19
	s_add_u32 s16, s24, s6
	s_addc_u32 s17, s25, s7
	s_add_i32 s28, s26, 0
	s_add_i32 m0, s28, 0x10000
	s_add_i32 s29, s28, 0x2000
	global_load_lds_dwordx4 v132, s[16:17]
	s_add_i32 m0, s28, 0x12000
	v_add_lshl_u32 v136, v2, v10, 1
	global_load_lds_dwordx4 v130, s[16:17]
	s_mov_b32 m0, s28
	s_add_u32 s6, s16, 0x40000
	global_load_lds_dwordx4 v134, s[8:9]
	s_mov_b32 m0, s29
	s_addc_u32 s7, s17, 0
	global_load_lds_dwordx4 v136, s[8:9]
	s_add_i32 m0, s28, 0x14000
	s_add_i32 s30, s28, 0x4000
	global_load_lds_dwordx4 v132, s[6:7]
	s_add_i32 m0, s28, 0x16000
	v_add_lshl_u32 v138, v146, s5, 1
	v_add_u32_e32 v2, s5, v12
	global_load_lds_dwordx4 v130, s[6:7]
	s_mov_b32 m0, s30
	s_add_i32 s31, s28, 0x6000
	v_add_lshl_u32 v140, v2, v10, 1
	global_load_lds_dwordx4 v138, s[8:9]
	s_mov_b32 m0, s31
	v_mov_b32_e32 v133, v227
	global_load_lds_dwordx4 v140, s[8:9]
	v_mov_b32_e32 v131, v227
	v_mov_b32_e32 v135, v227
	v_mov_b32_e32 v137, v227
	v_lshl_add_u64 v[8:9], s[16:17], 0, v[132:133]
	v_lshl_add_u64 v[6:7], s[16:17], 0, v[130:131]
	v_lshl_add_u64 v[4:5], s[8:9], 0, v[134:135]
	s_cmp_lg_u32 s1, 1
	v_lshl_add_u64 v[2:3], s[8:9], 0, v[136:137]
	s_cbranch_scc1 .LBB0_264
	s_barrier
	s_setprio 1

.LBB0_272:
	s_setprio 0
	s_barrier

.LBB0_419:
	s_or_b64 exec, exec, s[0:1]
	s_mov_b64 s[4:5], s[72:73]
	s_mov_b32 s0, s2
	v_mov_b32_e32 v7, v0
	s_waitcnt lgkmcnt(0)
	s_barrier
	s_cmpk_gt_i32 s0, 0x3b7
	v_readfirstlane_b32 s16, v7
	s_cbranch_scc1 .LBB0_439
	v_bfe_i32 v4, v7, 27, 1
	v_lshlrev_b32_e32 v2, 4, v7
	v_lshrrev_b32_e32 v4, 22, v4
	v_add_u32_e32 v4, v2, v4
	v_and_b32_e32 v4, 0xfffffc00, v4
	v_ashrrev_i32_e32 v3, 31, v7
	v_sub_u32_e32 v4, v2, v4
	v_lshrrev_b32_e32 v3, 26, v3
	v_lshrrev_b32_e32 v5, 4, v4
	v_add_u32_e32 v3, v7, v3
	v_bitop3_b32 v5, v5, v4, 32 bitop3:0x6c
	v_ashrrev_i32_e32 v4, 31, v4
	v_ashrrev_i32_e32 v3, 6, v3
	v_lshrrev_b32_e32 v4, 26, v4
	v_lshlrev_b32_e32 v6, 3, v3
	v_add_u32_e32 v4, v5, v4
	v_and_b32_e32 v6, -16, v6
	v_ashrrev_i32_e32 v4, 6, v4
	v_add_u32_e32 v46, v4, v6
	v_mul_i32_i24_e32 v6, 64, v4
	v_lshlrev_b32_e32 v3, 5, v3
	v_sub_u32_e32 v5, v5, v6
	v_and_b32_e32 v3, 32, v3
	v_ashrrev_i16_sdwa v5, v1, sext(v5) dst_sel:DWORD dst_unused:UNUSED_PAD src0_sel:DWORD src1_sel:BYTE_0
	v_add_u32_e32 v2, 0x2000, v2
	v_add_u32_sdwa v47, v3, sext(v5) dst_sel:DWORD dst_unused:UNUSED_PAD src0_sel:DWORD src1_sel:WORD_0
	v_ashrrev_i32_e32 v3, 31, v2
	v_lshrrev_b32_e32 v3, 22, v3
	v_add_u32_e32 v3, v2, v3
	v_ashrrev_i32_e32 v3, 10, v3
	v_mul_i32_i24_e32 v5, 0x400, v3
	v_sub_u32_e32 v2, v2, v5
	v_lshrrev_b32_e32 v5, 4, v2
	v_bitop3_b32 v2, v5, v2, 32 bitop3:0x6c
	v_ashrrev_i32_e32 v6, 31, v2
	v_lshrrev_b32_e32 v6, 26, v6
	s_load_dwordx4 s[8:11], s[4:5], 0x1d0
	s_load_dwordx2 s[12:13], s[4:5], 0x1b0
	v_lshlrev_b32_e32 v5, 3, v3
	v_add_u32_e32 v6, v2, v6
	v_and_b32_e32 v5, -16, v5
	v_ashrrev_i32_e32 v8, 6, v6
	v_readlane_b32 s4, v255, 12
	v_add_u32_e32 v48, v8, v5
	v_and_b32_e32 v5, 0xc0, v6
	s_mul_hi_u32 s1, s4, 0x150000
	s_mul_i32 s4, s4, 0x150000
	v_lshlrev_b32_e32 v3, 5, v3
	v_sub_u32_e32 v2, v2, v5
	s_waitcnt lgkmcnt(0)
	s_add_u32 s17, s8, s4
	v_and_b32_e32 v3, 32, v3
	v_ashrrev_i16_sdwa v2, v1, sext(v2) dst_sel:DWORD dst_unused:UNUSED_PAD src0_sel:DWORD src1_sel:BYTE_0
	s_addc_u32 s18, s9, s1
	v_add_u32_sdwa v49, v3, sext(v2) dst_sel:DWORD dst_unused:UNUSED_PAD src0_sel:DWORD src1_sel:WORD_0
	v_and_b32_e32 v2, 3, v8
	s_mov_b32 s1, 0x1ffffe0
	v_lshrrev_b32_e32 v3, 2, v48
	v_lshlrev_b32_e32 v5, 1, v48
	v_and_or_b32 v2, v48, s1, v2
	v_and_b32_e32 v3, 4, v3
	v_and_b32_e32 v5, 24, v5
	v_or3_b32 v2, v2, v3, v5
	s_movk_i32 s20, 0x180
	v_mul_lo_u32 v2, v2, s20
	v_add_lshl_u32 v34, v2, v49, 1
	v_and_b32_e32 v2, 3, v4
	v_and_or_b32 v2, v46, s1, v2
	s_ashr_i32 s1, s0, 31
	s_lshr_b32 s6, s1, 29
	v_readlane_b32 s5, v255, 13
	s_add_i32 s6, s0, s6
	s_ashr_i32 s5, s16, 6
	s_ashr_i32 s7, s6, 3
	s_and_b32 s6, s6, -8
	s_ashr_i32 s4, s16, 8
	s_lshl_b32 s19, s5, 10
	s_sub_i32 s6, s0, s6
	s_cmp_lt_i32 s6, 0
	s_movk_i32 s8, 0x78
	s_cselect_b32 s8, s8, 0x77
	s_mul_i32 s6, s8, s6
	s_add_i32 s6, s6, s7
	s_mul_hi_i32 s7, s6, 0x92492493
	s_add_i32 s7, s7, s6
	s_lshr_b32 s8, s7, 31
	s_ashr_i32 s7, s7, 5
	s_add_i32 s7, s7, s8
	s_lshl_b32 s8, s7, 3
	s_mul_i32 s7, s7, 56
	s_sub_i32 s7, s6, s7
	s_bfe_i32 s6, s7, 0x80000
	s_bfe_u32 s6, s6, 0x3000c
	s_add_i32 s9, s7, s6
	s_bfe_i32 s6, s9, 0x80000
	s_and_b32 s9, s9, 0xf8
	s_sub_i32 s9, s7, s9
	s_sext_i32_i8 s9, s9
	s_sext_i32_i16 s14, s6
	s_add_i32 s30, s8, s9
	v_lshrrev_b32_e32 v3, 2, v46
	v_lshlrev_b32_e32 v4, 1, v46
	s_lshr_b32 s6, s14, 3
	s_lshl_b32 s15, s30, 8
	v_and_b32_e32 v3, 4, v3
	v_and_b32_e32 v4, 24, v4
	s_cmp_gt_i32 s7, 15
	v_or3_b32 v2, v2, v3, v4
	s_cselect_b64 s[8:9], -1, 0
	v_mul_lo_u32 v2, v2, s20
	s_and_b64 s[8:9], s[8:9], exec
	v_add_lshl_u32 v36, v2, v47, 1
	s_cselect_b32 s8, 0x80, 0
	v_add_u32_e32 v2, s15, v46
	v_mul_lo_u32 v2, v2, s20
	v_add_u32_e32 v3, s8, v47
	v_add_lshl_u32 v4, v2, v3, 1
	v_add_u32_e32 v2, s15, v48
	s_bitset1_b32 s15, 7
	v_add_u32_e32 v6, s15, v46
	v_mul_lo_u32 v6, v6, s20
	s_ashr_i32 s7, s14, 3
	v_add_lshl_u32 v226, v6, v3, 1
	v_add_u32_e32 v3, s15, v48
	s_mul_hi_i32 s15, s7, 0x18000
	s_mul_i32 s14, s7, 0x18000
	s_mov_b32 s9, s56
	v_add_u32_e32 v5, s8, v49
	s_or_b64 s[8:9], s[14:15], s[8:9]
	s_lshl_b64 s[8:9], s[8:9], 1
	s_add_u32 s14, s17, s8
	v_mul_lo_u32 v2, v2, s20
	v_mul_lo_u32 v3, v3, s20
	s_addc_u32 s15, s18, s9
	s_add_i32 s20, s19, 0
	s_add_i32 m0, s20, 0x10000
	s_add_i32 s21, s20, 0x2000
	global_load_lds_dwordx4 v36, s[14:15]
	s_add_i32 m0, s20, 0x12000
	v_add_lshl_u32 v2, v5, v2, 1
	global_load_lds_dwordx4 v34, s[14:15]
	s_mov_b32 m0, s20
	s_add_u32 s8, s14, 0x18000
	global_load_lds_dwordx4 v4, s[12:13]
	s_mov_b32 m0, s21
	s_addc_u32 s9, s15, 0
	global_load_lds_dwordx4 v2, s[12:13]
	s_add_i32 m0, s20, 0x14000
	s_add_i32 s22, s20, 0x4000
	global_load_lds_dwordx4 v36, s[8:9]
	s_add_i32 m0, s20, 0x16000
	s_add_i32 s23, s20, 0x6000
	global_load_lds_dwordx4 v34, s[8:9]
	s_mov_b32 m0, s22
	v_add_lshl_u32 v6, v3, v5, 1
	global_load_lds_dwordx4 v226, s[12:13]
	s_mov_b32 m0, s23
	v_mov_b32_e32 v37, v227
	global_load_lds_dwordx4 v6, s[12:13]
	v_mov_b32_e32 v35, v227
	v_mov_b32_e32 v5, v227
	v_mov_b32_e32 v3, v227
	s_movk_i32 s43, 0x180
	v_lshl_add_u64 v[14:15], s[14:15], 0, v[36:37]
	v_lshl_add_u64 v[12:13], s[14:15], 0, v[34:35]
	v_lshl_add_u64 v[10:11], s[12:13], 0, v[4:5]
	s_cmp_lg_u32 s4, 1
	v_lshl_add_u64 v[8:9], s[12:13], 0, v[2:3]
	s_cbranch_scc1 .LBB0_422
	s_barrier
	s_setprio 1

.LBB0_981:
	v_mov_b32_e32 v10, v0
	s_cmp_ge_i32 s26, s12
	v_readfirstlane_b32 s27, v10
	s_cbranch_scc1 .LBB0_995
	v_lshlrev_b32_e32 v2, 4, v10
	v_add_u32_e32 v3, 0x2000, v2
	v_ashrrev_i32_e32 v4, 31, v3
	v_lshrrev_b32_e32 v4, 22, v4
	v_add_u32_e32 v4, v3, v4
	v_ashrrev_i32_e32 v4, 10, v4
	v_mul_i32_i24_e32 v6, 0x400, v4
	v_sub_u32_e32 v3, v3, v6
	v_lshrrev_b32_e32 v6, 4, v3
	v_bitop3_b32 v3, v6, v3, 32 bitop3:0x6c
	v_ashrrev_i32_e32 v6, 31, v3
	v_lshrrev_b32_e32 v6, 26, v6
	v_add_u32_e32 v6, v3, v6
	v_bfe_i32 v8, v10, 27, 1
	v_ashrrev_i32_e32 v7, 6, v6
	v_and_b32_e32 v6, 0xc0, v6
	v_lshrrev_b32_e32 v8, 22, v8
	v_lshlrev_b32_e32 v5, 5, v4
	v_sub_u32_e32 v3, v3, v6
	v_add_u32_e32 v8, v2, v8
	v_and_b32_e32 v5, 32, v5
	v_ashrrev_i16_sdwa v3, v1, sext(v3) dst_sel:DWORD dst_unused:UNUSED_PAD src0_sel:DWORD src1_sel:BYTE_0
	v_and_b32_e32 v8, 0xfffffc00, v8
	v_add_u32_sdwa v3, v5, sext(v3) dst_sel:DWORD dst_unused:UNUSED_PAD src0_sel:DWORD src1_sel:WORD_0
	v_ashrrev_i32_e32 v5, 31, v10
	v_sub_u32_e32 v2, v2, v8
	v_lshrrev_b32_e32 v5, 26, v5
	v_lshrrev_b32_e32 v8, 4, v2
	v_readlane_b32 s16, v255, 12
	v_add_u32_e32 v5, v10, v5
	v_bitop3_b32 v8, v8, v2, 32 bitop3:0x6c
	v_ashrrev_i32_e32 v2, 31, v2
	s_ashr_i32 s14, s27, 6
	v_readlane_b32 s17, v255, 13
	v_ashrrev_i32_e32 v5, 6, v5
	v_lshrrev_b32_e32 v2, 26, v2
	s_ashr_i32 s7, s27, 8
	s_lshl_b32 s28, s14, 10
	s_lshl_b64 s[16:17], s[16:17], 21
	v_lshlrev_b32_e32 v6, 5, v5
	v_add_u32_e32 v2, v8, v2
	v_lshlrev_b32_e32 v4, 3, v4
	v_lshlrev_b32_e32 v5, 3, v5
	s_waitcnt lgkmcnt(0)
	s_add_u32 s29, s0, s16
	v_ashrrev_i32_e32 v2, 6, v2
	v_and_b32_e32 v4, -16, v4
	v_and_b32_e32 v5, -16, v5
	s_addc_u32 s30, s1, s17
	v_mul_i32_i24_e32 v9, 64, v2
	v_add_u32_e32 v4, v7, v4
	v_and_b32_e32 v7, 3, v7
	s_mov_b32 s0, 0x1fffe0
	v_add_u32_e32 v5, v2, v5
	v_and_b32_e32 v2, 3, v2
	s_ashr_i32 s34, s26, 31
	v_and_or_b32 v7, v4, s0, v7
	v_and_or_b32 v2, v5, s0, v2
	s_lshr_b32 s0, s34, 29
	s_add_i32 s0, s26, s0
	s_lshr_b32 s31, s25, 1
	s_ashr_i32 s1, s0, 3
	s_and_b32 s0, s0, -8
	s_sub_i32 s0, s26, s0
	s_or_b32 s35, s31, 1
	s_cmp_lt_i32 s0, 0
	s_cselect_b32 s6, s35, s31
	s_mul_i32 s0, s6, s0
	s_add_i32 s0, s0, s1
	v_sub_u32_e32 v8, v8, v9
	s_ashr_i32 s1, s0, 31
	v_and_b32_e32 v6, 32, v6
	v_ashrrev_i16_sdwa v8, v1, sext(v8) dst_sel:DWORD dst_unused:UNUSED_PAD src0_sel:DWORD src1_sel:BYTE_0
	s_lshr_b32 s1, s1, 27
	v_add_u32_sdwa v6, v6, sext(v8) dst_sel:DWORD dst_unused:UNUSED_PAD src0_sel:DWORD src1_sel:WORD_0
	v_lshrrev_b32_e32 v8, 2, v4
	v_lshlrev_b32_e32 v9, 1, v4
	s_add_i32 s1, s0, s1
	v_and_b32_e32 v8, 4, v8
	v_and_b32_e32 v9, 24, v9
	s_ashr_i32 s6, s1, 5
	v_or3_b32 v7, v7, v8, v9
	v_lshlrev_b32_e32 v8, 1, v3
	s_lshl_b32 s15, s6, 3
	v_lshl_add_u32 v172, v7, 11, v8
	v_lshrrev_b32_e32 v7, 2, v5
	v_lshlrev_b32_e32 v8, 1, v5
	s_sub_i32 s6, s25, s15
	v_and_b32_e32 v7, 4, v7
	v_and_b32_e32 v8, 24, v8
	s_min_i32 s16, s6, 8
	v_or3_b32 v2, v2, v7, v8
	v_lshlrev_b32_e32 v7, 1, v6
	s_sext_i32_i8 s6, s16
	v_lshl_add_u32 v174, v2, 11, v7
	v_cvt_f32_i32_e32 v2, s6
	s_andn2_b32 s1, s1, 31
	s_sub_i32 s17, s0, s1
	v_cvt_f32_i32_e32 v7, s17
	v_rcp_iflag_f32_e32 v8, v2
	s_xor_b32 s0, s17, s6
	s_ashr_i32 s0, s0, 30
	s_or_b32 s6, s0, 1
	v_mul_f32_e32 v8, v7, v8
	v_trunc_f32_e32 v8, v8
	v_fma_f32 v7, -v8, v2, v7
	v_cvt_i32_f32_e32 v8, v8
	v_cmp_ge_f32_e64 s[0:1], |v7|, |v2|
	s_and_b64 s[0:1], s[0:1], exec
	s_cselect_b32 s0, s6, 0
	v_readfirstlane_b32 s1, v8
	s_add_i32 s6, s1, s0
	s_mul_i32 s0, s6, s16
	s_sub_i32 s0, s17, s0
	s_sext_i32_i8 s0, s0
	s_add_i32 s47, s15, s0
	s_lshl_b32 s0, s47, 18
	v_lshl_add_u32 v171, v5, 10, v6
	v_lshl_add_u32 v200, v4, 10, v3
	v_add_lshl_u32 v122, s0, v171, 1
	v_add_lshl_u32 v124, s0, v200, 1
	s_bitset1_b32 s0, 17
	v_add_lshl_u32 v128, s0, v171, 1
	v_add_lshl_u32 v126, s0, v200, 1
	s_bfe_i64 s[0:1], s[6:7], 0x80000
	s_lshl_b64 s[0:1], s[0:1], 19
	s_add_u32 s0, s29, s0
	s_addc_u32 s1, s30, s1
	s_add_i32 s36, s28, 0
	s_add_i32 m0, s36, 0x10000
	s_add_i32 s37, s36, 0x2000
	global_load_lds_dwordx4 v174, s[0:1]
	s_add_i32 m0, s36, 0x12000
	s_add_u32 s16, s0, 0x40000
	global_load_lds_dwordx4 v172, s[0:1]
	s_mov_b32 m0, s36
	s_addc_u32 s17, s1, 0
	global_load_lds_dwordx4 v122, s[8:9]
	s_mov_b32 m0, s37
	s_add_i32 s38, s36, 0x4000
	global_load_lds_dwordx4 v124, s[8:9]
	s_add_i32 m0, s36, 0x14000
	s_add_i32 s39, s36, 0x6000
	global_load_lds_dwordx4 v174, s[16:17]
	s_add_i32 m0, s36, 0x16000
	v_mov_b32_e32 v175, v227
	global_load_lds_dwordx4 v172, s[16:17]
	s_mov_b32 m0, s38
	v_mov_b32_e32 v173, v227
	global_load_lds_dwordx4 v128, s[8:9]
	s_mov_b32 m0, s39
	v_mov_b32_e32 v123, v227
	global_load_lds_dwordx4 v126, s[8:9]
	v_mov_b32_e32 v125, v227
	s_mov_b32 s13, s56
	v_lshl_add_u64 v[8:9], s[0:1], 0, v[174:175]
	v_lshl_add_u64 v[6:7], s[0:1], 0, v[172:173]
	v_lshl_add_u64 v[4:5], s[8:9], 0, v[122:123]
	s_cmp_lg_u32 s7, 1
	v_lshl_add_u64 v[2:3], s[8:9], 0, v[124:125]
	s_cbranch_scc1 .LBB0_984
	s_barrier
	s_setprio 1

.LBB0_994:
	s_setprio 0
	v_readlane_b32 s38, v255, 29
	v_readlane_b32 s39, v255, 30
	s_barrier

.LBB0_1230:
	v_mul_i32_i24_e32 v13, 64, v3
	v_sub_u32_e32 v6, v6, v13
	v_lshlrev_b32_e32 v5, 5, v5
	v_ashrrev_i16_sdwa v6, v1, sext(v6) dst_sel:DWORD dst_unused:UNUSED_PAD src0_sel:DWORD src1_sel:BYTE_0
	v_and_b32_e32 v5, 32, v5
	v_bfe_i32 v6, v6, 0, 16
	v_add_lshl_u32 v148, v5, v6, 1
	v_lshlrev_b32_e32 v6, 6, v4
	v_sub_u32_e32 v6, v8, v6
	v_lshlrev_b32_e32 v5, 5, v7
	v_ashrrev_i16_sdwa v6, v1, sext(v6) dst_sel:DWORD dst_unused:UNUSED_PAD src0_sel:DWORD src1_sel:BYTE_0
	v_and_b32_e32 v5, 32, v5
	v_bfe_i32 v6, v6, 0, 16
	v_add_lshl_u32 v149, v5, v6, 1
	v_lshlrev_b32_e32 v5, 1, v146
	v_lshrrev_b32_e32 v6, 2, v146
	v_and_b32_e32 v3, 3, v3
	s_mov_b32 s1, 0x1fffe0
	v_and_b32_e32 v5, 24, v5
	v_and_b32_e32 v6, 4, v6
	v_and_or_b32 v3, v146, s1, v3
	v_or3_b32 v3, v3, v6, v5
	v_lshl_add_u32 v130, v3, 11, v148
	v_lshlrev_b32_e32 v3, 1, v147
	v_lshrrev_b32_e32 v5, 2, v147
	v_and_b32_e32 v4, 3, v4
	v_and_b32_e32 v3, 24, v3
	v_and_b32_e32 v5, 4, v5
	v_and_or_b32 v4, v147, s1, v4
	v_or3_b32 v3, v4, v5, v3
	v_mov_b32_e32 v4, s6
	s_mov_b32 s9, s56
	v_readfirstlane_b32 s8, v4
	s_ashr_i32 s5, s27, 6
	s_ashr_i32 s1, s0, 31
	s_bfe_i64 s[8:9], s[8:9], 0x80000
	s_ashr_i32 s4, s27, 8
	s_lshl_b32 s30, s5, 10
	s_lshl_b64 s[8:9], s[8:9], 19
	s_lshl_b64 s[0:1], s[0:1], 22
	s_add_u32 s0, s12, s0
	s_addc_u32 s1, s13, s1
	s_add_u32 s0, s0, s8
	s_addc_u32 s1, s1, s9
	s_add_i32 s31, s30, 0
	s_add_i32 m0, s31, 0x10000
	v_lshl_add_u32 v132, v3, 11, v149
	global_load_lds_dwordx4 v130, s[0:1]
	s_add_i32 m0, s31, 0x12000
	s_waitcnt vmcnt(0)
	v_lshl_add_u32 v140, v9, 11, v148
	global_load_lds_dwordx4 v132, s[0:1]
	s_mov_b32 m0, s31
	s_add_i32 s34, s31, 0x2000
	v_lshl_add_u32 v138, v10, 11, v149
	global_load_lds_dwordx4 v140, s[10:11]
	s_mov_b32 m0, s34
	s_add_u32 s8, s0, 0x40000
	global_load_lds_dwordx4 v138, s[10:11]
	s_addc_u32 s9, s1, 0
	s_add_i32 m0, s31, 0x14000
	s_add_i32 s35, s31, 0x4000
	global_load_lds_dwordx4 v130, s[8:9]
	s_add_i32 m0, s31, 0x16000
	v_lshl_add_u32 v136, v11, 11, v148
	global_load_lds_dwordx4 v132, s[8:9]
	s_mov_b32 m0, s35
	s_add_i32 s36, s31, 0x6000
	v_lshl_add_u32 v134, v12, 11, v149
	global_load_lds_dwordx4 v136, s[10:11]
	s_mov_b32 m0, s36
	s_cmp_lg_u32 s4, 1
	global_load_lds_dwordx4 v134, s[10:11]
	s_cbranch_scc1 .LBB0_1232
	s_barrier
	s_setprio 1

.LBB0_1315:
	v_bfe_i32 v4, v10, 27, 1
	v_lshlrev_b32_e32 v2, 4, v10
	v_lshrrev_b32_e32 v4, 22, v4
	v_add_u32_e32 v4, v2, v4
	v_and_b32_e32 v4, 0xfffffc00, v4
	v_sub_u32_e32 v4, v2, v4
	v_lshrrev_b32_e32 v5, 4, v4
	v_bitop3_b32 v5, v5, v4, 32 bitop3:0x6c
	v_ashrrev_i32_e32 v4, 31, v4
	v_ashrrev_i32_e32 v3, 31, v10
	v_lshrrev_b32_e32 v4, 26, v4
	v_lshrrev_b32_e32 v3, 26, v3
	v_add_u32_e32 v4, v5, v4
	v_add_u32_e32 v3, v10, v3
	v_ashrrev_i32_e32 v4, 6, v4
	v_ashrrev_i32_e32 v3, 6, v3
	v_mul_i32_i24_e32 v7, 64, v4
	v_lshlrev_b32_e32 v6, 3, v3
	v_lshlrev_b32_e32 v3, 5, v3
	v_sub_u32_e32 v5, v5, v7
	v_and_b32_e32 v3, 32, v3
	v_ashrrev_i16_sdwa v5, v1, sext(v5) dst_sel:DWORD dst_unused:UNUSED_PAD src0_sel:DWORD src1_sel:BYTE_0
	v_add_u32_e32 v2, 0x2000, v2
	v_add_u32_sdwa v3, v3, sext(v5) dst_sel:DWORD dst_unused:UNUSED_PAD src0_sel:DWORD src1_sel:WORD_0
	v_ashrrev_i32_e32 v5, 31, v2
	v_lshrrev_b32_e32 v5, 22, v5
	v_add_u32_e32 v5, v2, v5
	v_ashrrev_i32_e32 v5, 10, v5
	v_mul_i32_i24_e32 v7, 0x400, v5
	v_sub_u32_e32 v2, v2, v7
	v_lshrrev_b32_e32 v7, 4, v2
	v_bitop3_b32 v2, v7, v2, 32 bitop3:0x6c
	v_ashrrev_i32_e32 v8, 31, v2
	v_lshrrev_b32_e32 v8, 26, v8
	v_add_u32_e32 v8, v2, v8
	v_ashrrev_i32_e32 v9, 6, v8
	v_and_b32_e32 v8, 0xc0, v8
	v_lshlrev_b32_e32 v7, 3, v5
	v_lshlrev_b32_e32 v5, 5, v5
	v_sub_u32_e32 v2, v2, v8
	v_and_b32_e32 v6, -16, v6
	v_and_b32_e32 v7, -16, v7
	v_and_b32_e32 v5, 32, v5
	v_ashrrev_i16_sdwa v2, v1, sext(v2) dst_sel:DWORD dst_unused:UNUSED_PAD src0_sel:DWORD src1_sel:BYTE_0
	v_add_u32_e32 v6, v4, v6
	v_add_u32_e32 v7, v9, v7
	v_add_u32_sdwa v2, v5, sext(v2) dst_sel:DWORD dst_unused:UNUSED_PAD src0_sel:DWORD src1_sel:WORD_0
	s_lshl_b32 s1, s46, 18
	v_lshl_add_u32 v146, v6, 10, v3
	v_lshl_add_u32 v147, v7, 10, v2
	v_add_lshl_u32 v134, s1, v146, 1
	v_add_lshl_u32 v136, s1, v147, 1
	s_bitset1_b32 s1, 17
	v_add_lshl_u32 v140, s1, v146, 1
	v_add_lshl_u32 v138, s1, v147, 1
	v_lshlrev_b32_e32 v5, 1, v6
	v_lshrrev_b32_e32 v8, 2, v6
	v_and_b32_e32 v4, 3, v4
	s_mov_b32 s1, 0x1fffe0
	v_and_b32_e32 v5, 24, v5
	v_and_b32_e32 v8, 4, v8
	v_and_or_b32 v4, v6, s1, v4
	v_or3_b32 v4, v4, v8, v5
	v_lshlrev_b32_e32 v3, 1, v3
	v_lshl_add_u32 v130, v4, 11, v3
	v_lshlrev_b32_e32 v3, 1, v7
	v_lshrrev_b32_e32 v4, 2, v7
	v_and_b32_e32 v5, 3, v9
	v_and_b32_e32 v3, 24, v3
	v_and_b32_e32 v4, 4, v4
	v_and_or_b32 v5, v7, s1, v5
	v_or3_b32 v3, v5, v4, v3
	v_lshlrev_b32_e32 v2, 1, v2
	v_lshl_add_u32 v132, v3, 11, v2
	v_mov_b32_e32 v2, s6
	s_mov_b32 s19, s56
	v_readfirstlane_b32 s18, v2
	s_ashr_i32 s5, s30, 6
	s_ashr_i32 s1, s0, 31
	s_bfe_i64 s[18:19], s[18:19], 0x80000
	s_ashr_i32 s4, s30, 8
	s_lshl_b32 s36, s5, 10
	s_lshl_b64 s[18:19], s[18:19], 19
	s_lshl_b64 s[0:1], s[0:1], 21
	s_waitcnt lgkmcnt(0)
	s_add_u32 s0, s14, s0
	s_addc_u32 s1, s15, s1
	s_add_u32 s22, s0, s18
	s_addc_u32 s23, s1, s19
	s_add_i32 s37, s36, 0
	s_add_i32 m0, s37, 0x10000
	s_add_i32 s38, s37, 0x2000
	global_load_lds_dwordx4 v130, s[22:23]
	s_add_i32 m0, s37, 0x12000
	s_add_u32 s0, s22, 0x40000
	global_load_lds_dwordx4 v132, s[22:23]
	s_mov_b32 m0, s37
	s_addc_u32 s1, s23, 0
	global_load_lds_dwordx4 v134, s[8:9]
	s_mov_b32 m0, s38
	s_add_i32 s39, s37, 0x4000
	global_load_lds_dwordx4 v136, s[8:9]
	s_add_i32 m0, s37, 0x14000
	s_add_i32 s40, s37, 0x6000
	global_load_lds_dwordx4 v130, s[0:1]
	s_add_i32 m0, s37, 0x16000
	v_mov_b32_e32 v131, v227
	global_load_lds_dwordx4 v132, s[0:1]
	s_mov_b32 m0, s39
	v_mov_b32_e32 v133, v227
	global_load_lds_dwordx4 v140, s[8:9]
	s_mov_b32 m0, s40
	v_mov_b32_e32 v135, v227
	global_load_lds_dwordx4 v138, s[8:9]
	v_mov_b32_e32 v137, v227
	v_lshl_add_u64 v[8:9], s[22:23], 0, v[130:131]
	v_lshl_add_u64 v[6:7], s[22:23], 0, v[132:133]
	v_lshl_add_u64 v[4:5], s[8:9], 0, v[134:135]
	s_cmp_lg_u32 s4, 1
	v_lshl_add_u64 v[2:3], s[8:9], 0, v[136:137]
	s_cbranch_scc1 .LBB0_1317
	s_barrier
	s_setprio 1
